# DIFF loop: packed row-sum clusters kept but split into two independent chains (no pads); GQA as before; MLA even-cost interleave
# speedup vs baseline: 1.0055x; 1.0021x over previous
.LBB0_952:
	s_lshr_b32 s11, s19, 3
	s_and_b32 s10, s19, 31
	s_and_b32 s11, s11, 0xffffe0
	s_or_b32 s10, s11, s10
	s_bfe_u32 s25, s19, 0x10007
	s_lshl_b32 s10, s10, 8
	s_bfe_u32 s26, s19, 0x20005
	s_lshl_b32 s11, s25, 14
	s_ashr_i32 s20, s10, 31
	s_add_u32 s10, s10, s11
	s_addc_u32 s11, s20, 0
	s_lshl_b64 s[20:21], s[10:11], 9
	s_add_u32 s22, s12, s20
	s_addc_u32 s21, s13, s21
	s_lshl_b32 s20, s26, 6
	s_lshl_b32 s23, s26, 7
	s_add_u32 s22, s22, s23
	s_addc_u32 s23, s21, 0
	s_lshl_b32 s21, s25, 2
	s_or_b32 s21, s21, s26
	s_mul_i32 s21, s21, 0x208000
	s_add_u32 s25, s14, s21
	s_addc_u32 s26, s15, 0
	v_mov_b32_e32 v4, v230
	s_add_u32 s27, s16, s21
	s_addc_u32 s28, s17, 0
	v_readfirstlane_b32 s21, v4
	v_and_b32_e32 v18, 31, v4
	s_ashr_i32 s21, s21, 6
	s_cmp_lt_i32 s21, 8
	v_lshl_or_b32 v0, s21, 5, v18
	v_ashrrev_i32_e32 v2, 31, v0
	s_cselect_b64 vcc, -1, 0
	v_cndmask_b32_e32 v3, 0, v2, vcc
	v_cndmask_b32_e32 v2, v18, v0, vcc
	v_bfe_u32 v5, v4, 5, 1
	v_lshlrev_b64 v[2:3], 9, v[2:3]
	v_lshl_add_u64 v[2:3], s[22:23], 0, v[2:3]
	v_lshlrev_b32_e32 v0, 4, v5
	v_lshl_add_u64 v[2:3], v[2:3], 0, v[0:1]
	global_load_dwordx4 v[130:133], v[2:3], off
	global_load_dwordx4 v[134:137], v[2:3], off offset:64
	global_load_dwordx4 v[138:141], v[2:3], off offset:32
	global_load_dwordx4 v[142:145], v[2:3], off offset:96
	s_lshl_b32 s29, s21, 10
	s_ashr_i32 s30, s29, 31
	v_and_b32_e32 v0, 63, v4
	v_and_b32_e32 v2, 19, v4
	v_lshlrev_b32_e32 v3, 1, v4
	v_lshrrev_b32_e32 v4, 1, v4
	s_add_u32 s22, s25, s29
	v_and_b32_e32 v3, 8, v3
	v_and_b32_e32 v4, 4, v4
	s_addc_u32 s23, s26, s30
	s_add_i32 s21, s29, 0
	v_lshlrev_b32_e32 v19, 10, v5
	v_or3_b32 v2, v2, v3, v4
	v_lshlrev_b32_e32 v0, 4, v0
	s_add_u32 s26, s27, s29
	s_mov_b32 m0, s21
	v_lshl_or_b32 v2, v2, 4, v19
	v_lshl_add_u64 v[174:175], s[22:23], 0, v[0:1]
	global_load_lds_dwordx4 v0, s[22:23]
	s_addc_u32 s27, s28, s30
	s_add_i32 m0, s21, 0x2000
	s_mov_b64 s[22:23], 0x2000
	v_add_u32_e32 v188, 0, v2
	v_lshl_add_u64 v[176:177], s[26:27], 0, v[0:1]
	global_load_lds_dwordx4 v0, s[26:27]
	v_lshl_add_u64 v[2:3], v[174:175], 0, s[22:23]
	s_add_i32 m0, s21, 0x4000
	v_mov_b32_e32 v150, v1
	global_load_lds_dwordx4 v[2:3], off
	v_lshl_add_u64 v[2:3], v[176:177], 0, s[22:23]
	s_add_i32 m0, s21, 0x6000
	v_lshl_or_b32 v0, v18, 4, v19
	global_load_lds_dwordx4 v[2:3], off
	s_waitcnt vmcnt(0)
	s_waitcnt vmcnt(0) lgkmcnt(0)
	s_barrier
	ds_read_b128 v[2:5], v188
	ds_read_b128 v[6:9], v188 offset:4096
	ds_read_b128 v[98:101], v188 offset:512
	ds_read_b128 v[10:13], v188 offset:2048
	ds_read_b128 v[102:105], v188 offset:4608
	ds_read_b128 v[14:17], v188 offset:6144
	ds_read_b128 v[162:165], v188 offset:2560
	ds_read_b128 v[166:169], v188 offset:6656
	s_mov_b32 s22, 2
	s_mov_b32 s23, 1
	s_mov_b32 s27, 0
	s_mov_b32 s25, 0
	s_mov_b32 s26, 0
	v_add_u32_e32 v0, 0, v0
	v_mov_b32_e32 v151, v150
	v_mov_b32_e32 v152, v150
	v_mov_b32_e32 v153, v150
	v_mov_b32_e32 v154, v150
	v_mov_b32_e32 v155, v150
	v_mov_b32_e32 v156, v150
	v_mov_b32_e32 v157, v150
	s_waitcnt lgkmcnt(7)
	v_mfma_f32_32x32x16_bf16 v[82:97], v[2:5], v[130:133], 0
	v_mov_b32_e32 v2, 0
	v_mov_b32_e32 v3, v2
	v_mov_b32_e32 v4, v2
	v_mov_b32_e32 v5, v2
	v_mov_b32_e32 v18, v2
	v_mov_b32_e32 v19, v2
	v_mov_b32_e32 v20, v2
	s_waitcnt lgkmcnt(6)
	v_mfma_f32_32x32x16_bf16 v[66:81], v[6:9], v[134:137], 0
	v_mov_b32_e32 v6, v2
	v_mov_b32_e32 v7, v2
	v_mov_b32_e32 v8, v2
	v_mov_b32_e32 v9, v2
	v_mov_b32_e32 v21, v2
	v_mov_b32_e32 v22, v2
	v_mov_b32_e32 v23, v2
	s_waitcnt lgkmcnt(4)
	v_mfma_f32_32x32x16_bf16 v[82:97], v[10:13], v[138:141], v[82:97]
	v_mov_b32_e32 v10, v2
	v_mov_b32_e32 v11, v2
	v_mov_b32_e32 v12, v2
	v_mov_b32_e32 v13, v2
	v_mov_b32_e32 v24, v2
	v_mov_b32_e32 v25, v2
	v_mov_b32_e32 v26, v2
	s_waitcnt lgkmcnt(2)
	v_mfma_f32_32x32x16_bf16 v[66:81], v[14:17], v[142:145], v[66:81]
	v_mov_b32_e32 v14, v2
	v_mov_b32_e32 v15, v2
	v_mov_b32_e32 v16, v2
	v_mov_b32_e32 v17, v2
	v_mov_b32_e32 v27, v2
	v_mov_b32_e32 v28, v2
	v_mov_b32_e32 v29, v2
	v_mov_b32_e32 v30, v2
	v_mov_b32_e32 v31, v2
	v_mov_b32_e32 v32, v2
	v_mov_b32_e32 v33, v2
	v_mov_b32_e32 v158, v150
	v_mov_b32_e32 v159, v150
	v_mov_b32_e32 v160, v150
	v_mov_b32_e32 v161, v150
	v_mov_b32_e32 v146, v150
	v_mov_b32_e32 v147, v150
	v_mov_b32_e32 v148, v150
	v_mov_b32_e32 v149, v150
	v_mov_b32_e32 v34, v2
	v_mov_b32_e32 v35, v2
	v_mov_b32_e32 v36, v2
	v_mov_b32_e32 v37, v2
	v_mov_b32_e32 v38, v2
	v_mov_b32_e32 v39, v2
	v_mov_b32_e32 v40, v2
	v_mov_b32_e32 v41, v2
	v_mov_b32_e32 v42, v2
	v_mov_b32_e32 v43, v2
	v_mov_b32_e32 v44, v2
	v_mov_b32_e32 v45, v2
	v_mov_b32_e32 v46, v2
	v_mov_b32_e32 v47, v2
	v_mov_b32_e32 v48, v2
	v_mov_b32_e32 v49, v2
	v_mov_b32_e32 v50, v2
	v_mov_b32_e32 v51, v2
	v_mov_b32_e32 v52, v2
	v_mov_b32_e32 v53, v2
	v_mov_b32_e32 v54, v2
	v_mov_b32_e32 v55, v2
	v_mov_b32_e32 v56, v2
	v_mov_b32_e32 v57, v2
	v_mov_b32_e32 v58, v2
	v_mov_b32_e32 v59, v2
	v_mov_b32_e32 v60, v2
	v_mov_b32_e32 v61, v2
	v_mov_b32_e32 v62, v2
	v_mov_b32_e32 v63, v2
	v_mov_b32_e32 v64, v2
	v_mov_b32_e32 v65, v2
	v_mov_b32_e32 v178, v2
	v_mov_b32_e32 v179, v2
	v_mov_b32_e32 v234, 0
	v_mov_b32_e32 v235, 0
.LBB0_953:
	s_min_i32 s28, s26, 0x101
	s_lshl_b32 s28, s28, 13
	s_add_i32 s88, s28, 0x4000
	s_lshl_b32 s28, s22, 14
	s_add_i32 s28, s21, s28
	v_lshl_add_u64 v[106:107], v[174:175], 0, s[88:89]
	s_mov_b32 m0, s28
	v_lshl_add_u32 v181, s27, 14, v0
	global_load_lds_dwordx4 v[106:107], off
	v_lshl_add_u64 v[106:107], v[176:177], 0, s[88:89]
	s_add_i32 m0, s28, 0x2000
	s_lshl_b32 s28, s25, 14
	global_load_lds_dwordx4 v[106:107], off
	ds_read_b128 v[190:193], v181 offset:12288
	v_add_u32_e32 v189, s28, v0
	v_lshl_add_u32 v210, s23, 14, v188
	v_mfma_f32_32x32x16_bf16 v[114:129], v[98:101], v[130:133], 0
	v_exp_f32_e32 v194, v82
	v_exp_f32_e32 v196, v83
	v_exp_f32_e32 v198, v84
	v_exp_f32_e32 v200, v85
	v_mfma_f32_32x32x16_bf16 v[98:113], v[102:105], v[134:137], 0
	ds_read_b128 v[82:85], v181 offset:12800
	v_cvt_pk_bf16_f32 v170, v194, v196
	v_cvt_pk_bf16_f32 v171, v198, v200
	v_exp_f32_e32 v202, v86
	v_exp_f32_e32 v204, v87
	s_waitcnt lgkmcnt(0)
	v_mfma_f32_32x32x16_bf16 v[114:129], v[162:165], v[138:141], v[114:129]
	v_cvt_pk_bf16_f32 v172, v202, v204
	v_exp_f32_e32 v206, v88
	v_exp_f32_e32 v208, v89
	v_mfma_f32_32x32x16_bf16 v[98:113], v[166:169], v[142:145], v[98:113]
	v_exp_f32_e32 v168, v92
	v_exp_f32_e32 v166, v93
	v_cvt_pk_bf16_f32 v173, v206, v208
	v_exp_f32_e32 v214, v90
	v_exp_f32_e32 v216, v91
	v_mfma_f32_32x32x16_bf16 v[34:49], v[190:193], v[150:153], v[34:49]
	ds_read_b128 v[86:89], v181 offset:14336
	v_cvt_pk_bf16_f32 v162, v214, v216
	v_cvt_pk_bf16_f32 v163, v168, v166
	v_exp_f32_e32 v182, v94
	v_exp_f32_e32 v180, v95
	v_mfma_f32_32x32x16_bf16 v[50:65], v[82:85], v[150:153], v[50:65]
	ds_read_b128 v[90:93], v181 offset:14848
	v_cvt_pk_bf16_f32 v164, v182, v180
	v_exp_f32_e32 v186, v96
	v_exp_f32_e32 v184, v97
	v_mfma_f32_32x32x16_bf16 v[2:17], v[190:193], v[158:161], v[2:17]
	v_cvt_pk_bf16_f32 v165, v186, v184
	v_exp_f32_e32 v195, v66
	v_exp_f32_e32 v197, v67
	v_exp_f32_e32 v199, v68
	v_exp_f32_e32 v201, v69
	v_mfma_f32_32x32x16_bf16 v[18:33], v[82:85], v[158:161], v[18:33]
	v_cvt_pk_bf16_f32 v158, v195, v197
	v_cvt_pk_bf16_f32 v159, v199, v201
	v_exp_f32_e32 v203, v70
	v_exp_f32_e32 v205, v71
	s_waitcnt lgkmcnt(0)
	v_mfma_f32_32x32x16_bf16 v[34:49], v[86:89], v[154:157], v[34:49]
	ds_read_b128 v[66:69], v210
	v_cvt_pk_bf16_f32 v160, v203, v205
	v_exp_f32_e32 v207, v72
	v_exp_f32_e32 v209, v73
	v_mfma_f32_32x32x16_bf16 v[50:65], v[90:93], v[154:157], v[50:65]
	ds_read_b128 v[70:73], v210 offset:4096
	v_exp_f32_e32 v169, v76
	v_exp_f32_e32 v167, v77
	v_cvt_pk_bf16_f32 v161, v207, v209
	v_exp_f32_e32 v215, v74
	v_exp_f32_e32 v217, v75
	v_pk_add_f32 v[74:75], v[178:179], v[194:195]
	v_mfma_f32_32x32x16_bf16 v[2:17], v[86:89], v[146:149], v[2:17]
	v_add_f32_e64 v74, v196, v74
	v_add_f32_e64 v75, v197, v75
	ds_read_b128 v[152:155], v210 offset:2048
	v_add_f32_e64 v74, v198, v74
	v_add_f32_e64 v75, v199, v75
	v_cvt_pk_bf16_f32 v190, v215, v217
	v_pk_add_f32 v[234:235], v[200:201], v[234:235]
	v_cvt_pk_bf16_f32 v191, v169, v167
	v_pk_add_f32 v[74:75], v[202:203], v[74:75]
	v_exp_f32_e32 v183, v78
	v_pk_add_f32 v[234:235], v[204:205], v[234:235]
	v_exp_f32_e32 v181, v79
	v_pk_add_f32 v[74:75], v[206:207], v[74:75]
	v_pk_add_f32 v[234:235], v[208:209], v[234:235]
	v_pk_add_f32 v[74:75], v[214:215], v[74:75]
	s_nop 0
	v_pk_add_f32 v[178:179], v[216:217], v[74:75]
	v_mfma_f32_32x32x16_bf16 v[18:33], v[90:93], v[146:149], v[18:33]
	v_exp_f32_e32 v187, v80
	v_exp_f32_e32 v185, v81
	ds_read_b128 v[194:197], v210 offset:6144
	v_cvt_pk_bf16_f32 v192, v183, v181
	v_cvt_pk_bf16_f32 v193, v187, v185
	s_waitcnt lgkmcnt(0)
	v_mfma_f32_32x32x16_bf16 v[82:97], v[66:69], v[130:133], 0
	ds_read_b128 v[146:149], v189 offset:8192
	v_exp_f32_e32 v198, v114
	v_exp_f32_e32 v200, v115
	v_exp_f32_e32 v202, v116
	v_exp_f32_e32 v204, v117
	v_mfma_f32_32x32x16_bf16 v[66:81], v[70:73], v[134:137], 0
	ds_read_b128 v[114:117], v189 offset:8704
	v_cvt_pk_bf16_f32 v150, v198, v200
	v_cvt_pk_bf16_f32 v151, v202, v204
	v_exp_f32_e32 v206, v118
	v_exp_f32_e32 v208, v119
	v_mfma_f32_32x32x16_bf16 v[82:97], v[152:155], v[138:141], v[82:97]
	v_cvt_pk_bf16_f32 v152, v206, v208
	v_exp_f32_e32 v214, v120
	v_exp_f32_e32 v216, v121
	v_mfma_f32_32x32x16_bf16 v[66:81], v[194:197], v[142:145], v[66:81]
	v_cvt_pk_bf16_f32 v153, v214, v216
	v_exp_f32_e32 v194, v122
	v_exp_f32_e32 v196, v123
	v_exp_f32_e32 v218, v124
	v_exp_f32_e32 v220, v125
	s_waitcnt lgkmcnt(0)
	v_mfma_f32_32x32x16_bf16 v[34:49], v[146:149], v[170:173], v[34:49]
	ds_read_b128 v[118:121], v189 offset:10240
	v_cvt_pk_bf16_f32 v154, v194, v196
	v_cvt_pk_bf16_f32 v155, v218, v220
	v_exp_f32_e32 v126, v126
	v_exp_f32_e32 v222, v127
	v_mfma_f32_32x32x16_bf16 v[50:65], v[114:117], v[170:173], v[50:65]
	ds_read_b128 v[122:125], v189 offset:10752
	v_cvt_pk_bf16_f32 v156, v126, v222
	v_exp_f32_e32 v128, v128
	v_exp_f32_e32 v170, v129
	v_mfma_f32_32x32x16_bf16 v[2:17], v[146:149], v[158:161], v[2:17]
	v_cvt_pk_bf16_f32 v157, v128, v170
	v_exp_f32_e32 v199, v98
	v_exp_f32_e32 v201, v99
	v_exp_f32_e32 v203, v100
	v_exp_f32_e32 v205, v101
	v_mfma_f32_32x32x16_bf16 v[18:33], v[114:117], v[158:161], v[18:33]
	v_cvt_pk_bf16_f32 v158, v199, v201
	v_cvt_pk_bf16_f32 v159, v203, v205
	v_exp_f32_e32 v207, v102
	v_exp_f32_e32 v209, v103
	v_pk_add_f32 v[102:103], v[168:169], v[178:179]
	s_waitcnt lgkmcnt(0)
	v_mfma_f32_32x32x16_bf16 v[34:49], v[118:121], v[162:165], v[34:49]
	v_add_f32_e64 v102, v166, v102
	v_add_f32_e64 v103, v167, v103
	ds_read_b128 v[98:101], v210 offset:512
	v_add_f32_e64 v102, v182, v102
	v_add_f32_e64 v103, v183, v103
	v_cvt_pk_bf16_f32 v160, v207, v209
	v_pk_add_f32 v[234:235], v[180:181], v[234:235]
	v_exp_f32_e32 v215, v104
	v_pk_add_f32 v[102:103], v[186:187], v[102:103]
	v_exp_f32_e32 v217, v105
	v_pk_add_f32 v[234:235], v[184:185], v[234:235]
	v_pk_add_f32 v[102:103], v[102:103], v[198:199]
	v_pk_add_f32 v[234:235], v[200:201], v[234:235]
	v_pk_add_f32 v[102:103], v[202:203], v[102:103]
	v_pk_add_f32 v[234:235], v[204:205], v[234:235]
	v_pk_add_f32 v[114:115], v[206:207], v[102:103]
	v_mfma_f32_32x32x16_bf16 v[50:65], v[122:125], v[162:165], v[50:65]
	ds_read_b128 v[102:105], v210 offset:4608
	v_cvt_pk_bf16_f32 v161, v215, v217
	v_exp_f32_e32 v195, v106
	v_exp_f32_e32 v197, v107
	v_exp_f32_e32 v219, v108
	v_exp_f32_e32 v221, v109
	v_mfma_f32_32x32x16_bf16 v[2:17], v[118:121], v[190:193], v[2:17]
	ds_read_b128 v[162:165], v210 offset:2560
	v_cvt_pk_bf16_f32 v146, v195, v197
	v_cvt_pk_bf16_f32 v147, v219, v221
	v_exp_f32_e32 v127, v110
	v_exp_f32_e32 v223, v111
	v_pk_add_f32 v[106:107], v[208:209], v[114:115]
	v_mfma_f32_32x32x16_bf16 v[18:33], v[122:125], v[190:193], v[18:33]
	v_add_f32_e64 v106, v214, v106
	v_add_f32_e64 v107, v215, v107
	v_exp_f32_e32 v129, v112
	v_pk_add_f32 v[106:107], v[216:217], v[106:107]
	ds_read_b128 v[166:169], v210 offset:6656
	v_pk_add_f32 v[234:235], v[194:195], v[234:235]
	v_exp_f32_e32 v171, v113
	v_pk_add_f32 v[106:107], v[196:197], v[106:107]
	v_cvt_pk_bf16_f32 v148, v127, v223
	v_pk_add_f32 v[234:235], v[218:219], v[234:235]
	v_cvt_pk_bf16_f32 v149, v129, v171
	v_pk_add_f32 v[106:107], v[220:221], v[106:107]
	v_pk_add_f32 v[234:235], v[126:127], v[234:235]
	v_pk_add_f32 v[106:107], v[222:223], v[106:107]
	v_pk_add_f32 v[234:235], v[128:129], v[234:235]
	v_pk_add_f32 v[178:179], v[170:171], v[106:107]
	s_add_i32 s27, s22, 1
	s_waitcnt vmcnt(0)
	s_and_b32 s28, s27, 3
	s_add_i32 s26, s26, 1
	s_cmpk_eq_i32 s26, 0x104
	s_mov_b32 s27, s25
	s_mov_b32 s25, s23
	s_mov_b32 s23, s22
	s_mov_b32 s22, s28
	s_waitcnt vmcnt(0) lgkmcnt(0)
	s_barrier
	s_cbranch_scc0 .LBB0_953
	v_add_f32_e32 v178, v178, v234
	v_add_f32_e32 v179, v179, v235
	ds_read_b128 v[66:69], v189 offset:12288
	ds_read_b128 v[70:73], v189 offset:12800
	v_mov_b32_e32 v0, v230
	s_waitcnt lgkmcnt(1)
	v_mfma_f32_32x32x16_bf16 v[34:49], v[66:69], v[150:153], v[34:49]
	s_waitcnt lgkmcnt(0)
	v_mfma_f32_32x32x16_bf16 v[50:65], v[70:73], v[150:153], v[50:65]
	v_mfma_f32_32x32x16_bf16 v[2:17], v[66:69], v[158:161], v[2:17]
	v_mfma_f32_32x32x16_bf16 v[18:33], v[70:73], v[158:161], v[18:33]
	ds_read_b128 v[68:71], v189 offset:14336
	ds_read_b128 v[72:75], v189 offset:14848
	v_mbcnt_lo_u32_b32 v76, -1, 0
	v_mbcnt_hi_u32_b32 v76, -1, v76
	v_mbcnt_lo_u32_b32 v77, -1, 0
	v_mbcnt_hi_u32_b32 v77, -1, v77
	global_load_dwordx2 v[66:67], v1, s[6:7]
	v_lshlrev_b32_e32 v77, 2, v77
	v_xor_b32_e32 v77, 0x80, v77
	v_lshlrev_b32_e32 v76, 2, v76
	ds_bpermute_b32 v77, v77, v179
	v_xor_b32_e32 v76, 0x80, v76
	ds_bpermute_b32 v76, v76, v178
	s_waitcnt lgkmcnt(3)
	v_mfma_f32_32x32x16_bf16 v[2:17], v[68:71], v[146:149], v[2:17]
	v_readfirstlane_b32 s21, v0
	s_ashr_i32 s21, s21, 1
	s_andn2_b32 s21, s21, 31
	s_cmpk_lt_i32 s21, 0x100
	s_waitcnt lgkmcnt(2)
	v_mfma_f32_32x32x16_bf16 v[18:33], v[72:75], v[146:149], v[18:33]
	v_mfma_f32_32x32x16_bf16 v[34:49], v[68:71], v[154:157], v[34:49]
	s_waitcnt lgkmcnt(1)
	v_add_f32_e32 v70, v179, v77
	v_mbcnt_lo_u32_b32 v68, -1, 0
	v_mbcnt_hi_u32_b32 v68, -1, v68
	v_rcp_f32_e32 v70, v70
	v_lshlrev_b32_e32 v69, 2, v68
	s_waitcnt lgkmcnt(0)
	v_add_f32_e32 v68, v178, v76
	v_rcp_f32_e32 v68, v68
	s_waitcnt vmcnt(0)
	v_mul_f32_e32 v66, v66, v70
	v_mfma_f32_32x32x16_bf16 v[50:65], v[72:75], v[154:157], v[50:65]
	v_mul_f32_e64 v2, v2, v66
	v_mul_f32_e64 v3, v3, v66
	v_mul_f32_e64 v18, v18, v66
	v_mul_f32_e64 v19, v19, v66
	v_mul_f32_e64 v4, v4, v66
	v_mul_f32_e64 v5, v5, v66
	v_pk_mul_f32 v[20:21], v[20:21], v[66:67] op_sel_hi:[1,0]
	v_pk_mul_f32 v[70:71], v[24:25], v[66:67] op_sel_hi:[1,0]
	v_pk_fma_f32 v[24:25], v[34:35], v[68:69], v[2:3] op_sel_hi:[1,0,1] neg_lo:[0,0,1] neg_hi:[0,0,1]
	v_pk_mul_f32 v[72:73], v[26:27], v[66:67] op_sel_hi:[1,0]
	s_nop 1
	v_pk_fma_f32 v[2:3], v[50:51], v[68:69], v[18:19] op_sel_hi:[1,0,1] neg_lo:[0,0,1] neg_hi:[0,0,1]
	v_pk_fma_f32 v[26:27], v[36:37], v[68:69], v[4:5] op_sel_hi:[1,0,1] neg_lo:[0,0,1] neg_hi:[0,0,1]
	v_pk_fma_f32 v[4:5], v[52:53], v[68:69], v[20:21] op_sel_hi:[1,0,1] neg_lo:[0,0,1] neg_hi:[0,0,1]
	v_pk_mul_f32 v[18:19], v[2:3], v[2:3]
	v_pk_mul_f32 v[6:7], v[6:7], v[66:67] op_sel_hi:[1,0]
	v_pk_mul_f32 v[22:23], v[22:23], v[66:67] op_sel_hi:[1,0]
	v_pk_mul_f32 v[36:37], v[4:5], v[4:5]
	v_pk_fma_f32 v[18:19], v[24:25], v[24:25], v[18:19]
	v_pk_mul_f32 v[74:75], v[28:29], v[66:67] op_sel_hi:[1,0]
	v_pk_fma_f32 v[28:29], v[38:39], v[68:69], v[6:7] op_sel_hi:[1,0,1] neg_lo:[0,0,1] neg_hi:[0,0,1]
	v_pk_fma_f32 v[6:7], v[54:55], v[68:69], v[22:23] op_sel_hi:[1,0,1] neg_lo:[0,0,1] neg_hi:[0,0,1]
	v_pk_fma_f32 v[36:37], v[26:27], v[26:27], v[36:37]
	v_add_f32_e32 v18, v18, v19
	v_pk_mul_f32 v[8:9], v[8:9], v[66:67] op_sel_hi:[1,0]
	v_pk_mul_f32 v[38:39], v[6:7], v[6:7]
	v_add_f32_e32 v18, v36, v18
	v_pk_mul_f32 v[76:77], v[30:31], v[66:67] op_sel_hi:[1,0]
	v_pk_fma_f32 v[30:31], v[40:41], v[68:69], v[8:9] op_sel_hi:[1,0,1] neg_lo:[0,0,1] neg_hi:[0,0,1]
	v_pk_fma_f32 v[8:9], v[56:57], v[68:69], v[70:71] op_sel_hi:[1,0,1] neg_lo:[0,0,1] neg_hi:[0,0,1]
	v_pk_fma_f32 v[38:39], v[28:29], v[28:29], v[38:39]
	v_add_f32_e32 v18, v37, v18
	v_pk_mul_f32 v[10:11], v[10:11], v[66:67] op_sel_hi:[1,0]
	v_pk_mul_f32 v[40:41], v[8:9], v[8:9]
	v_add_f32_e32 v18, v38, v18
	v_pk_mul_f32 v[78:79], v[32:33], v[66:67] op_sel_hi:[1,0]
	v_pk_fma_f32 v[32:33], v[42:43], v[68:69], v[10:11] op_sel_hi:[1,0,1] neg_lo:[0,0,1] neg_hi:[0,0,1]
	v_pk_fma_f32 v[10:11], v[58:59], v[68:69], v[72:73] op_sel_hi:[1,0,1] neg_lo:[0,0,1] neg_hi:[0,0,1]
	v_pk_fma_f32 v[40:41], v[30:31], v[30:31], v[40:41]
	v_add_f32_e32 v18, v39, v18
	v_pk_mul_f32 v[12:13], v[12:13], v[66:67] op_sel_hi:[1,0]
	v_pk_mul_f32 v[42:43], v[10:11], v[10:11]
	v_add_f32_e32 v18, v40, v18
	v_pk_fma_f32 v[34:35], v[44:45], v[68:69], v[12:13] op_sel_hi:[1,0,1] neg_lo:[0,0,1] neg_hi:[0,0,1]
	v_pk_fma_f32 v[12:13], v[60:61], v[68:69], v[74:75] op_sel_hi:[1,0,1] neg_lo:[0,0,1] neg_hi:[0,0,1]
	v_pk_fma_f32 v[42:43], v[32:33], v[32:33], v[42:43]
	v_add_f32_e32 v18, v41, v18
	v_pk_mul_f32 v[14:15], v[14:15], v[66:67] op_sel_hi:[1,0]
	v_pk_mul_f32 v[44:45], v[12:13], v[12:13]
	v_add_f32_e32 v18, v42, v18
	v_pk_fma_f32 v[20:21], v[46:47], v[68:69], v[14:15] op_sel_hi:[1,0,1] neg_lo:[0,0,1] neg_hi:[0,0,1]
	v_pk_fma_f32 v[14:15], v[62:63], v[68:69], v[76:77] op_sel_hi:[1,0,1] neg_lo:[0,0,1] neg_hi:[0,0,1]
	v_pk_fma_f32 v[44:45], v[34:35], v[34:35], v[44:45]
	v_add_f32_e32 v18, v43, v18
	v_pk_mul_f32 v[16:17], v[16:17], v[66:67] op_sel_hi:[1,0]
	v_pk_mul_f32 v[46:47], v[14:15], v[14:15]
	v_add_f32_e32 v18, v44, v18
	v_pk_fma_f32 v[22:23], v[48:49], v[68:69], v[16:17] op_sel_hi:[1,0,1] neg_lo:[0,0,1] neg_hi:[0,0,1]
	v_pk_fma_f32 v[16:17], v[64:65], v[68:69], v[78:79] op_sel_hi:[1,0,1] neg_lo:[0,0,1] neg_hi:[0,0,1]
	v_pk_fma_f32 v[46:47], v[20:21], v[20:21], v[46:47]
	v_add_f32_e32 v18, v45, v18
	v_pk_mul_f32 v[48:49], v[16:17], v[16:17]
	v_add_f32_e32 v18, v46, v18
	v_pk_fma_f32 v[48:49], v[22:23], v[22:23], v[48:49]
	v_add_f32_e32 v18, v47, v18
	v_add_f32_e32 v18, v48, v18
	v_add_f32_e32 v36, v49, v18
	v_xor_b32_e32 v18, 0x80, v69
	ds_bpermute_b32 v37, v18, v36
	s_cbranch_scc0 .LBB0_951
	s_waitcnt lgkmcnt(0)
	v_add_f32_e32 v36, v36, v37
	v_fmamk_f32 v36, v36, 0x3c800000, v224
	v_cmp_gt_f32_e32 vcc, s31, v36
	v_mul_f32_e32 v37, 0x4b800000, v36
	v_and_or_b32 v18, v0, 31, s21
	v_cndmask_b32_e32 v36, v36, v37, vcc
	v_rsq_f32_e32 v36, v36
	v_lshrrev_b32_e32 v0, 3, v0
	v_and_b32_e32 v0, 4, v0
	v_lshlrev_b32_e32 v41, 2, v0
	v_mul_f32_e32 v37, 0x45800000, v36
	v_cndmask_b32_e32 v36, v36, v37, vcc
	v_mul_f32_e32 v40, v67, v36
	global_load_dwordx4 v[36:39], v41, s[8:9] offset:128
	s_lshl_b64 s[10:11], s[10:11], 11
	s_add_u32 s10, s2, s10
	s_addc_u32 s11, s3, s11
	s_lshl_b32 s20, s20, 1
	s_add_u32 s10, s10, s20
	v_ashrrev_i32_e32 v19, 31, v18
	s_addc_u32 s11, s11, 0
	v_lshlrev_b64 v[18:19], 11, v[18:19]
	v_lshl_add_u64 v[18:19], s[10:11], 0, v[18:19]
	v_lshlrev_b32_e32 v0, 1, v0
	v_lshl_add_u64 v[18:19], v[18:19], 0, v[0:1]
	s_waitcnt vmcnt(0)
	v_pk_mul_f32 v[36:37], v[40:41], v[36:37] op_sel_hi:[0,1]
	v_pk_mul_f32 v[2:3], v[2:3], v[36:37]
	v_pk_mul_f32 v[36:37], v[40:41], v[38:39] op_sel_hi:[0,1]
	v_pk_mul_f32 v[4:5], v[4:5], v[36:37]
	global_load_dwordx4 v[36:39], v41, s[8:9] offset:160
	v_cvt_pk_bf16_f32 v2, v2, v3
	v_cvt_pk_bf16_f32 v3, v4, v5
	s_waitcnt vmcnt(0)
	v_pk_mul_f32 v[36:37], v[40:41], v[36:37] op_sel_hi:[0,1]
	v_pk_mul_f32 v[6:7], v[6:7], v[36:37]
	v_pk_mul_f32 v[36:37], v[40:41], v[38:39] op_sel_hi:[0,1]
	v_pk_mul_f32 v[8:9], v[8:9], v[36:37]
	global_load_dwordx4 v[36:39], v41, s[8:9] offset:192
	v_cvt_pk_bf16_f32 v4, v6, v7
	v_cvt_pk_bf16_f32 v5, v8, v9
	s_waitcnt vmcnt(0)
	v_pk_mul_f32 v[36:37], v[40:41], v[36:37] op_sel_hi:[0,1]
	v_pk_mul_f32 v[10:11], v[10:11], v[36:37]
	v_pk_mul_f32 v[36:37], v[40:41], v[38:39] op_sel_hi:[0,1]
	v_pk_mul_f32 v[12:13], v[12:13], v[36:37]
	global_load_dwordx4 v[36:39], v41, s[8:9] offset:224
	s_waitcnt vmcnt(0)
	v_pk_mul_f32 v[36:37], v[40:41], v[36:37] op_sel_hi:[0,1]
	v_pk_mul_f32 v[14:15], v[14:15], v[36:37]
	v_pk_mul_f32 v[36:37], v[40:41], v[38:39] op_sel_hi:[0,1]
	v_pk_mul_f32 v[16:17], v[16:17], v[36:37]
	global_load_dwordx4 v[36:39], v41, s[8:9]
	s_waitcnt vmcnt(0)
	v_pk_mul_f32 v[36:37], v[40:41], v[36:37] op_sel_hi:[0,1]
	v_pk_mul_f32 v[24:25], v[24:25], v[36:37]
	v_pk_mul_f32 v[36:37], v[40:41], v[38:39] op_sel_hi:[0,1]
	v_pk_mul_f32 v[26:27], v[26:27], v[36:37]
	global_load_dwordx4 v[36:39], v41, s[8:9] offset:32
	v_cvt_pk_bf16_f32 v24, v24, v25
	v_cvt_pk_bf16_f32 v25, v26, v27
	s_waitcnt vmcnt(0)
	v_pk_mul_f32 v[36:37], v[40:41], v[36:37] op_sel_hi:[0,1]
	v_pk_mul_f32 v[28:29], v[28:29], v[36:37]
	v_pk_mul_f32 v[36:37], v[40:41], v[38:39] op_sel_hi:[0,1]
	v_pk_mul_f32 v[30:31], v[30:31], v[36:37]
	global_load_dwordx4 v[36:39], v41, s[8:9] offset:64
	s_waitcnt vmcnt(0)
	v_pk_mul_f32 v[36:37], v[40:41], v[36:37] op_sel_hi:[0,1]
	v_pk_mul_f32 v[32:33], v[32:33], v[36:37]
	v_pk_mul_f32 v[36:37], v[40:41], v[38:39] op_sel_hi:[0,1]
	v_pk_mul_f32 v[34:35], v[34:35], v[36:37]
	global_load_dwordx4 v[36:39], v41, s[8:9] offset:96
	s_nop 0
	global_store_dwordx2 v[18:19], v[24:25], off offset:1024
	global_store_dwordx2 v[18:19], v[2:3], off offset:1088
	v_cvt_pk_bf16_f32 v2, v28, v29
	v_cvt_pk_bf16_f32 v3, v30, v31
	global_store_dwordx2 v[18:19], v[2:3], off offset:1040
	global_store_dwordx2 v[18:19], v[4:5], off offset:1104
	v_cvt_pk_bf16_f32 v2, v32, v33
	v_cvt_pk_bf16_f32 v3, v34, v35
	v_cvt_pk_bf16_f32 v4, v10, v11
	v_cvt_pk_bf16_f32 v5, v12, v13
	global_store_dwordx2 v[18:19], v[2:3], off offset:1056
	global_store_dwordx2 v[18:19], v[4:5], off offset:1120
	v_cvt_pk_bf16_f32 v4, v14, v15
	v_cvt_pk_bf16_f32 v5, v16, v17
	s_waitcnt vmcnt(6)
	v_pk_mul_f32 v[36:37], v[40:41], v[36:37] op_sel_hi:[0,1]
	v_pk_mul_f32 v[20:21], v[20:21], v[36:37]
	v_pk_mul_f32 v[36:37], v[40:41], v[38:39] op_sel_hi:[0,1]
	v_pk_mul_f32 v[22:23], v[22:23], v[36:37]
	v_cvt_pk_bf16_f32 v2, v20, v21
	v_cvt_pk_bf16_f32 v3, v22, v23
	global_store_dwordx2 v[18:19], v[2:3], off offset:1072
	global_store_dwordx2 v[18:19], v[4:5], off offset:1136
	s_branch .LBB0_951
